# adds: hyena filter layers 1-2: weight columns kept in registers across elements and tasks, inputs read from LDS in bulk
# speedup vs baseline: 1.0159x; 1.0082x over previous
;     ...
;     const float* w1 = P.in[15]; const float* b1 = P.in[16]; const float* fq = P.in[17];
;     const float* w2 = P.in[18]; const float* b2 = P.in[19]; const float* w3 = P.in[20];
;     float* zemb = sm;
;     float* h1 = sm + 32 * 33;
;     float* h2 = h1 + 32 * 64;
;     const int tid = threadIdx.x;
;     __syncthreads();
;     for (int e = tid; e < 32 * 33; e += NTHR) {
;         const int pp = e / 33, i = e % 33;
;         const float pos = (float)(p0 + pp);
;         float v;
;         if (i == 0) v = pos / (float)(l - 1);
;         else {
;             const int b = (i - 1) & 15;
;             const float band = 1e-4f + (float)b * ((15.f - 1e-4f) / 15.f);
;             const float ang = ((float)(2.0 * 3.14159265358979323846 / (double)l) * pos) * band;
;             v = (i <= 16) ? cosf(ang) : -sinf(ang);
;         }
;         zemb[e] = v;
;     }
;     __syncthreads();
;     for (int e = tid; e < 32 * 64; e += NTHR) {
;         const int pp = e >> 6, j = e & 63;
;         float s = b1[j];
; #pragma unroll 4
;         for (int i = 0; i < 33; ++i) s += zemb[pp * 33 + i] * w1[i * 64 + j];
;         h1[e] = sinf(fq[j] * s);
;     }
;     __syncthreads();
;     for (int e = tid; e < 32 * 64; e += NTHR) {
;         const int pp = e >> 6, j = e & 63;
;         float s = b2[j];
; #pragma unroll 4
;         for (int i = 0; i < 64; ++i) s += h1[pp * 64 + i] * w2[i * 64 + j];
;         h2[e] = sinf(fq[j] * s);
;     }
;     __syncthreads();
;     const float lo = -4.605170185988091f / 1.5f, hi = -4.605170185988091f / 0.3f;
;     const float delta = fabsf(lo + (float)tid * ((hi - lo) / 511.f));
.LBB0_34:
	s_or_b64 exec, exec, s[0:1]
	s_cmpk_gt_i32 s44, 0x207
	s_cbranch_scc1 .LBB0_109
	v_cvt_f32_u32_e32 v2, v0
	v_readlane_b32 s12, v253, 51
	v_mul_u32_u24_e32 v3, 0x208, v0
	v_lshlrev_b32_e32 v6, 2, v202
	v_mov_b32_e32 v7, 0
	v_readlane_b32 s13, v253, 52
	v_readlane_b32 s14, v253, 53
	v_readlane_b32 s15, v253, 54
	v_readlane_b32 s18, v253, 57
	v_readlane_b32 s19, v253, 58
	v_readlane_b32 s0, v252, 19
	v_mov_b32_e32 v67, 0xc0447cbd
	v_lshl_add_u64 v[8:9], s[12:13], 0, v[6:7]
	v_lshl_add_u64 v[10:11], s[14:15], 0, v[6:7]
	v_lshl_add_u64 v[12:13], s[18:19], 0, v[6:7]
	v_lshlrev_b32_e32 v6, 2, v3
	v_readlane_b32 s1, v252, 20
	v_readlane_b32 s2, v252, 21
	v_readlane_b32 s3, v252, 22
	v_fmac_f32_e32 v67, 0xbcc4df2d, v2
	s_mov_b64 s[0:1], 0x40662400
	v_lshl_add_u64 v[2:3], s[2:3], 0, v[6:7]
	v_lshl_add_u64 v[14:15], v[2:3], 0, s[0:1]
	v_mul_u32_u24_e32 v3, 0x84, v1
	v_readlane_b32 s0, v253, 35
	v_add3_u32 v69, v3, 0, 16
	v_mov_b32_e32 v3, 0x200
	v_readlane_b32 s10, v253, 45
	v_readlane_b32 s11, v253, 46
	v_readlane_b32 s16, v253, 55
	v_readlane_b32 s17, v253, 56
	v_readlane_b32 s20, v253, 59
	v_readlane_b32 s21, v253, 60
	v_readlane_b32 s24, v253, 63
	v_readlane_b32 s25, v252, 0
	v_readlane_b32 s26, v252, 1
	v_readlane_b32 s27, v252, 2
	v_lshlrev_b32_e32 v2, 2, v0
	v_lshl_or_b32 v6, v202, 2, v3
	v_readlane_b32 s12, v253, 47
	v_readlane_b32 s13, v253, 48
	v_readlane_b32 s14, v253, 49
	v_readlane_b32 s15, v253, 50
	v_mov_b32_e32 v3, v7
	s_mov_b32 s10, 0x54442d18
	v_add3_u32 v68, v2, 0, 16
	v_lshl_add_u64 v[16:17], s[14:15], 0, v[6:7]
	v_lshl_add_u64 v[18:19], s[16:17], 0, v[6:7]
	v_lshl_add_u64 v[20:21], s[20:21], 0, v[2:3]
	s_mov_b32 s11, 0x401921fb
	v_mov_b32_e32 v23, 0x3f7fff90
	s_brev_b32 s24, 18
	s_mov_b32 s25, 0xfe5163ab
	s_mov_b32 s26, 0x3c439041
	s_mov_b32 s27, 0xdb629599
	s_mov_b32 s28, 0xf534ddc0
	s_mov_b32 s29, 0xfc2757d1
	s_mov_b32 s30, 0x4e441529
	s_mov_b32 s31, 0xa2f9836e
	s_mov_b32 s34, 0x3fc90fda
	s_mov_b32 s35, 0x3f22f983
	s_mov_b32 s36, 0xbfc90fda
	v_mov_b32_e32 v70, 0x3c0881c4
	v_mov_b32_e32 v71, 0xbab64f3b
	s_movk_i32 s37, 0x1f8
	s_mov_b64 s[12:13], 0x400
	s_movk_i32 s38, 0x5ff
	s_add_i32 s39, 0, 0x1090
	s_mov_b32 s40, 0x3fb8aa3b
	s_mov_b32 s41, 0xc2ce8ed0
	s_mov_b32 s42, 0x42b17218
	v_not_b32_e32 v72, 63
	v_not_b32_e32 v73, 31
	v_mov_b32_e32 v74, 0xffc00000
	v_mov_b32_e32 v75, 0x7fc00000
	v_mov_b32_e32 v76, 0x7f800000
	s_mov_b32 s14, s44
	v_readlane_b32 s22, v253, 61
	v_readlane_b32 s23, v253, 62
	v_readlane_b32 s1, v253, 36
	v_readlane_b32 s2, v253, 37
	v_readlane_b32 s3, v253, 38
	v_readlane_b32 s4, v253, 39
	v_readlane_b32 s5, v253, 40
	v_readlane_b32 s6, v253, 41
	v_readlane_b32 s7, v253, 42
	v_readlane_b32 s8, v253, 43
	v_readlane_b32 s9, v253, 44
	global_load_dword v104, v[16:17], off offset:-512
	global_load_dword v105, v[16:17], off offset:-256
	global_load_dword v106, v[16:17], off
	global_load_dword v107, v[16:17], off offset:256
	global_load_dword v108, v[16:17], off offset:512
	global_load_dword v109, v[16:17], off offset:768
	global_load_dword v110, v[16:17], off offset:1024
	global_load_dword v111, v[16:17], off offset:1280
	global_load_dword v112, v[16:17], off offset:1536
	global_load_dword v113, v[16:17], off offset:1792
	global_load_dword v114, v[16:17], off offset:2048
	global_load_dword v115, v[16:17], off offset:2304
	global_load_dword v116, v[16:17], off offset:2560
	global_load_dword v117, v[16:17], off offset:2816
	global_load_dword v118, v[16:17], off offset:3072
	global_load_dword v119, v[16:17], off offset:3328
	s_mov_b64 s[98:99], 0x1000
	v_lshl_add_u64 v[2:3], v[16:17], 0, s[98:99]
	global_load_dword v120, v[2:3], off offset:-512
	global_load_dword v121, v[2:3], off offset:-256
	global_load_dword v122, v[2:3], off
	global_load_dword v123, v[2:3], off offset:256
	global_load_dword v124, v[2:3], off offset:512
	global_load_dword v125, v[2:3], off offset:768
	global_load_dword v126, v[2:3], off offset:1024
;     ...
;     for (int e = tid; e < 32 * 64; e += NTHR) {
;         const int pp = e >> 6, j = e & 63;
;         float s = b1[j];
; #pragma unroll 4
;         for (int i = 0; i < 33; ++i) s += zemb[pp * 33 + i] * w1[i * 64 + j];
;         h1[e] = sinf(fq[j] * s);
;     }
;     __syncthreads();
;     for (int e = tid; e < 32 * 64; e += NTHR) {
;         const int pp = e >> 6, j = e & 63;
;         float s = b2[j];
; #pragma unroll 4
;         for (int i = 0; i < 64; ++i) s += h1[pp * 64 + i] * w2[i * 64 + j];
;         h2[e] = sinf(fq[j] * s);
	global_load_dword v127, v[2:3], off offset:1280
	global_load_dword v128, v[2:3], off offset:1536
	global_load_dword v129, v[2:3], off offset:1792
	global_load_dword v130, v[2:3], off offset:2048
	global_load_dword v131, v[2:3], off offset:2304
	global_load_dword v132, v[2:3], off offset:2560
	global_load_dword v133, v[2:3], off offset:2816
	global_load_dword v134, v[2:3], off offset:3072
	global_load_dword v135, v[2:3], off offset:3328
	s_mov_b64 s[98:99], 0x2000
	v_lshl_add_u64 v[2:3], v[16:17], 0, s[98:99]
	global_load_dword v136, v[2:3], off offset:-512
	global_load_dword v137, v[18:19], off offset:-512
	global_load_dword v138, v[18:19], off offset:-256
	global_load_dword v139, v[18:19], off
	global_load_dword v140, v[18:19], off offset:256
	global_load_dword v141, v[18:19], off offset:512
	global_load_dword v142, v[18:19], off offset:768
	global_load_dword v143, v[18:19], off offset:1024
	global_load_dword v144, v[18:19], off offset:1280
	global_load_dword v145, v[18:19], off offset:1536
	global_load_dword v146, v[18:19], off offset:1792
	global_load_dword v147, v[18:19], off offset:2048
	global_load_dword v148, v[18:19], off offset:2304
	global_load_dword v149, v[18:19], off offset:2560
	global_load_dword v150, v[18:19], off offset:2816
	global_load_dword v151, v[18:19], off offset:3072
	global_load_dword v152, v[18:19], off offset:3328
	s_mov_b64 s[98:99], 0x1000
	v_lshl_add_u64 v[2:3], v[18:19], 0, s[98:99]
	global_load_dword v153, v[2:3], off offset:-512
	global_load_dword v154, v[2:3], off offset:-256
	global_load_dword v155, v[2:3], off
	global_load_dword v156, v[2:3], off offset:256
	global_load_dword v157, v[2:3], off offset:512
	global_load_dword v158, v[2:3], off offset:768
	global_load_dword v159, v[2:3], off offset:1024
	global_load_dword v160, v[2:3], off offset:1280
	global_load_dword v161, v[2:3], off offset:1536
	global_load_dword v162, v[2:3], off offset:1792
	global_load_dword v163, v[2:3], off offset:2048
	global_load_dword v164, v[2:3], off offset:2304
	global_load_dword v165, v[2:3], off offset:2560
	global_load_dword v166, v[2:3], off offset:2816
	global_load_dword v167, v[2:3], off offset:3072
	global_load_dword v168, v[2:3], off offset:3328
	s_mov_b64 s[98:99], 0x2000
	v_lshl_add_u64 v[2:3], v[18:19], 0, s[98:99]
	global_load_dword v169, v[2:3], off offset:-512
	global_load_dword v170, v[2:3], off offset:-256
	global_load_dword v171, v[2:3], off
	global_load_dword v172, v[2:3], off offset:256
	global_load_dword v173, v[2:3], off offset:512
	global_load_dword v174, v[2:3], off offset:768
	global_load_dword v175, v[2:3], off offset:1024
	global_load_dword v176, v[2:3], off offset:1280
	global_load_dword v177, v[2:3], off offset:1536
	global_load_dword v178, v[2:3], off offset:1792
	global_load_dword v179, v[2:3], off offset:2048
	global_load_dword v180, v[2:3], off offset:2304
	global_load_dword v181, v[2:3], off offset:2560
	global_load_dword v182, v[2:3], off offset:2816
	global_load_dword v183, v[2:3], off offset:3072
	global_load_dword v184, v[2:3], off offset:3328
	s_mov_b64 s[98:99], 0x3000
	v_lshl_add_u64 v[2:3], v[18:19], 0, s[98:99]
	global_load_dword v185, v[2:3], off offset:-512
	global_load_dword v186, v[2:3], off offset:-256
	global_load_dword v187, v[2:3], off
	global_load_dword v188, v[2:3], off offset:256
	global_load_dword v189, v[2:3], off offset:512
	global_load_dword v190, v[2:3], off offset:768
	global_load_dword v191, v[2:3], off offset:1024
	global_load_dword v192, v[2:3], off offset:1280
	global_load_dword v193, v[2:3], off offset:1536
	global_load_dword v194, v[2:3], off offset:1792
	global_load_dword v195, v[2:3], off offset:2048
	global_load_dword v196, v[2:3], off offset:2304
	global_load_dword v197, v[2:3], off offset:2560
	global_load_dword v198, v[2:3], off offset:2816
	global_load_dword v199, v[2:3], off offset:3072
	global_load_dword v200, v[2:3], off offset:3328
	s_branch .LBB0_37

;     ...
;     for (int e = tid; e < 32 * 64; e += NTHR) {
;         const int pp = e >> 6, j = e & 63;
;         float s = b1[j];
; #pragma unroll 4
;         for (int i = 0; i < 33; ++i) s += zemb[pp * 33 + i] * w1[i * 64 + j];
;         h1[e] = sinf(fq[j] * s);
.LBB0_57:
	s_waitcnt vmcnt(0)
	ds_read2_b32 v[26:27], v22 offset0:0 offset1:1
	ds_read2_b32 v[28:29], v22 offset0:2 offset1:3
	ds_read2_b32 v[30:31], v22 offset0:4 offset1:5
	ds_read2_b32 v[32:33], v22 offset0:6 offset1:7
	ds_read2_b32 v[34:35], v22 offset0:8 offset1:9
	ds_read2_b32 v[36:37], v22 offset0:10 offset1:11
	ds_read2_b32 v[38:39], v22 offset0:12 offset1:13
	ds_read2_b32 v[40:41], v22 offset0:14 offset1:15
	ds_read2_b32 v[42:43], v22 offset0:16 offset1:17
	ds_read2_b32 v[44:45], v22 offset0:18 offset1:19
	ds_read2_b32 v[46:47], v22 offset0:20 offset1:21
	ds_read2_b32 v[48:49], v22 offset0:22 offset1:23
	ds_read2_b32 v[50:51], v22 offset0:24 offset1:25
	ds_read2_b32 v[52:53], v22 offset0:26 offset1:27
	ds_read2_b32 v[54:55], v22 offset0:28 offset1:29
	ds_read2_b32 v[56:57], v22 offset0:30 offset1:31
	ds_read_b32 v58, v22 offset:128
	v_mov_b32_e32 v6, v4
	s_waitcnt lgkmcnt(0)
	v_fmac_f32_e32 v6, v26, v104
	v_fmac_f32_e32 v6, v27, v105
	v_fmac_f32_e32 v6, v28, v106
	v_fmac_f32_e32 v6, v29, v107
	v_fmac_f32_e32 v6, v30, v108
	v_fmac_f32_e32 v6, v31, v109
	v_fmac_f32_e32 v6, v32, v110
	v_fmac_f32_e32 v6, v33, v111
	v_fmac_f32_e32 v6, v34, v112
	v_fmac_f32_e32 v6, v35, v113
	v_fmac_f32_e32 v6, v36, v114
	v_fmac_f32_e32 v6, v37, v115
	v_fmac_f32_e32 v6, v38, v116
	v_fmac_f32_e32 v6, v39, v117
	v_fmac_f32_e32 v6, v40, v118
	v_fmac_f32_e32 v6, v41, v119
	v_fmac_f32_e32 v6, v42, v120
	v_fmac_f32_e32 v6, v43, v121
	v_fmac_f32_e32 v6, v44, v122
	v_fmac_f32_e32 v6, v45, v123
	v_fmac_f32_e32 v6, v46, v124
	v_fmac_f32_e32 v6, v47, v125
	v_fmac_f32_e32 v6, v48, v126
	v_fmac_f32_e32 v6, v49, v127
	v_fmac_f32_e32 v6, v50, v128
	v_fmac_f32_e32 v6, v51, v129
	v_fmac_f32_e32 v6, v52, v130
	v_fmac_f32_e32 v6, v53, v131
	v_fmac_f32_e32 v6, v54, v132
	v_fmac_f32_e32 v6, v55, v133
	v_fmac_f32_e32 v6, v56, v134
	v_fmac_f32_e32 v6, v57, v135
	v_fmac_f32_e32 v6, v58, v136

;     ...
;     for (int e = tid; e < 32 * 64; e += NTHR) {
;         const int pp = e >> 6, j = e & 63;
;         float s = b2[j];
; #pragma unroll 4
;         for (int i = 0; i < 64; ++i) s += h1[pp * 64 + i] * w2[i * 64 + j];
;         h2[e] = sinf(fq[j] * s);
.LBB0_67:
	v_and_b32_e32 v2, 31, v22
	v_lshl_add_u32 v6, v2, 8, s39
	s_waitcnt vmcnt(0)
	v_mov_b32_e32 v25, v4
	ds_read_b128 v[26:29], v6 offset:0
	ds_read_b128 v[30:33], v6 offset:16
	ds_read_b128 v[34:37], v6 offset:32
	ds_read_b128 v[38:41], v6 offset:48
	ds_read_b128 v[42:45], v6 offset:64
	ds_read_b128 v[46:49], v6 offset:80
	ds_read_b128 v[50:53], v6 offset:96
	ds_read_b128 v[54:57], v6 offset:112
	s_waitcnt lgkmcnt(0)
	v_fmac_f32_e32 v25, v26, v137
	v_fmac_f32_e32 v25, v27, v138
	v_fmac_f32_e32 v25, v28, v139
	v_fmac_f32_e32 v25, v29, v140
	v_fmac_f32_e32 v25, v30, v141
	v_fmac_f32_e32 v25, v31, v142
	v_fmac_f32_e32 v25, v32, v143
	v_fmac_f32_e32 v25, v33, v144
	v_fmac_f32_e32 v25, v34, v145
	v_fmac_f32_e32 v25, v35, v146
	v_fmac_f32_e32 v25, v36, v147
	v_fmac_f32_e32 v25, v37, v148
	v_fmac_f32_e32 v25, v38, v149
	v_fmac_f32_e32 v25, v39, v150
	v_fmac_f32_e32 v25, v40, v151
	v_fmac_f32_e32 v25, v41, v152
	v_fmac_f32_e32 v25, v42, v153
	v_fmac_f32_e32 v25, v43, v154
	v_fmac_f32_e32 v25, v44, v155
	v_fmac_f32_e32 v25, v45, v156
	v_fmac_f32_e32 v25, v46, v157
	v_fmac_f32_e32 v25, v47, v158
	v_fmac_f32_e32 v25, v48, v159
	v_fmac_f32_e32 v25, v49, v160
	v_fmac_f32_e32 v25, v50, v161
	v_fmac_f32_e32 v25, v51, v162
	v_fmac_f32_e32 v25, v52, v163
	v_fmac_f32_e32 v25, v53, v164
	v_fmac_f32_e32 v25, v54, v165
	v_fmac_f32_e32 v25, v55, v166
	v_fmac_f32_e32 v25, v56, v167
	v_fmac_f32_e32 v25, v57, v168
	ds_read_b128 v[26:29], v6 offset:128
	ds_read_b128 v[30:33], v6 offset:144
	ds_read_b128 v[34:37], v6 offset:160
	ds_read_b128 v[38:41], v6 offset:176
	ds_read_b128 v[42:45], v6 offset:192
	ds_read_b128 v[46:49], v6 offset:208
	ds_read_b128 v[50:53], v6 offset:224
	ds_read_b128 v[54:57], v6 offset:240
	s_waitcnt lgkmcnt(0)
	v_fmac_f32_e32 v25, v26, v169
	v_fmac_f32_e32 v25, v27, v170
	v_fmac_f32_e32 v25, v28, v171
	v_fmac_f32_e32 v25, v29, v172
	v_fmac_f32_e32 v25, v30, v173
	v_fmac_f32_e32 v25, v31, v174
	v_fmac_f32_e32 v25, v32, v175
	v_fmac_f32_e32 v25, v33, v176
	v_fmac_f32_e32 v25, v34, v177
	v_fmac_f32_e32 v25, v35, v178
	v_fmac_f32_e32 v25, v36, v179
	v_fmac_f32_e32 v25, v37, v180
	v_fmac_f32_e32 v25, v38, v181
	v_fmac_f32_e32 v25, v39, v182
	v_fmac_f32_e32 v25, v40, v183
	v_fmac_f32_e32 v25, v41, v184
	v_fmac_f32_e32 v25, v42, v185
	v_fmac_f32_e32 v25, v43, v186
	v_fmac_f32_e32 v25, v44, v187
	v_fmac_f32_e32 v25, v45, v188
	v_fmac_f32_e32 v25, v46, v189
	v_fmac_f32_e32 v25, v47, v190
	v_fmac_f32_e32 v25, v48, v191
	v_fmac_f32_e32 v25, v49, v192
	v_fmac_f32_e32 v25, v50, v193
	v_fmac_f32_e32 v25, v51, v194
	v_fmac_f32_e32 v25, v52, v195
	v_fmac_f32_e32 v25, v53, v196
	v_fmac_f32_e32 v25, v54, v197
	v_fmac_f32_e32 v25, v55, v198
	v_fmac_f32_e32 v25, v56, v199
	v_fmac_f32_e32 v25, v57, v200
	v_mul_f32_e32 v2, v25, v5
	v_and_b32_e32 v3, 0x7fffffff, v2
	v_cmp_nlt_f32_e64 s[0:1], |v2|, s24
	s_and_saveexec_b64 s[6:7], s[0:1]
	s_xor_b64 s[16:17], exec, s[6:7]
	s_cbranch_execz .LBB0_71
	v_lshrrev_b32_e32 v6, 23, v3
	v_add_u32_e32 v6, 0xffffff88, v6
	v_cmp_lt_u32_e32 vcc, 63, v6
	s_nop 1
	v_cndmask_b32_e32 v25, 0, v72, vcc
	v_add_u32_e32 v6, v25, v6
	v_cmp_lt_u32_e64 s[0:1], 31, v6
	s_nop 1
	v_cndmask_b32_e64 v25, 0, v73, s[0:1]
	v_add_u32_e32 v6, v25, v6
	v_cmp_lt_u32_e64 s[6:7], 31, v6
	s_nop 1
	v_cndmask_b32_e64 v25, 0, v73, s[6:7]
	v_add_u32_e32 v25, v25, v6
	v_and_b32_e32 v6, 0x7fffff, v3
	v_or_b32_e32 v38, 0x800000, v6
	v_mad_u64_u32 v[26:27], s[8:9], v38, s25, 0
	v_mov_b32_e32 v6, v27
	v_mad_u64_u32 v[28:29], s[8:9], v38, s26, v[6:7]
	v_mov_b32_e32 v6, v29
	v_mad_u64_u32 v[30:31], s[8:9], v38, s27, v[6:7]
	v_mov_b32_e32 v6, v31
	v_mad_u64_u32 v[32:33], s[8:9], v38, s28, v[6:7]
	v_mov_b32_e32 v6, v33
	v_mad_u64_u32 v[34:35], s[8:9], v38, s29, v[6:7]
	v_mov_b32_e32 v6, v35
	v_mad_u64_u32 v[36:37], s[8:9], v38, s30, v[6:7]
	v_mov_b32_e32 v6, v37
	v_mad_u64_u32 v[38:39], s[8:9], v38, s31, v[6:7]
	v_cndmask_b32_e32 v27, v36, v32, vcc
	v_cndmask_b32_e32 v6, v38, v34, vcc
	v_cndmask_b32_e32 v31, v39, v36, vcc
	v_cndmask_b32_e64 v29, v6, v27, s[0:1]
	v_cndmask_b32_e64 v6, v31, v6, s[0:1]
	v_cndmask_b32_e32 v31, v34, v30, vcc
	v_cndmask_b32_e64 v27, v27, v31, s[0:1]
	v_sub_u32_e32 v33, 32, v25
	v_cmp_eq_u32_e64 s[8:9], 0, v25
	v_cndmask_b32_e32 v25, v32, v28, vcc
	v_cndmask_b32_e64 v6, v6, v29, s[6:7]
	v_cndmask_b32_e64 v29, v29, v27, s[6:7]
	v_cndmask_b32_e64 v28, v31, v25, s[0:1]
	v_alignbit_b32 v34, v6, v29, v33
	v_cndmask_b32_e64 v27, v27, v28, s[6:7]
	v_cndmask_b32_e64 v6, v34, v6, s[8:9]
	v_alignbit_b32 v31, v29, v27, v33
	v_cndmask_b32_e32 v26, v30, v26, vcc
	v_cndmask_b32_e64 v29, v31, v29, s[8:9]
	v_bfe_u32 v34, v6, 29, 1
	v_cndmask_b32_e64 v25, v25, v26, s[0:1]
	v_alignbit_b32 v31, v6, v29, 30
	v_sub_u32_e32 v35, 0, v34
	v_cndmask_b32_e64 v25, v28, v25, s[6:7]
	v_xor_b32_e32 v31, v31, v35
	v_alignbit_b32 v26, v27, v25, v33
	v_cndmask_b32_e64 v26, v26, v27, s[8:9]
	v_ffbh_u32_e32 v28, v31
	v_alignbit_b32 v27, v29, v26, 30
	v_min_u32_e32 v28, 32, v28
	v_alignbit_b32 v25, v26, v25, 30
	v_xor_b32_e32 v27, v27, v35
	v_sub_u32_e32 v29, 31, v28
	v_xor_b32_e32 v25, v25, v35
	v_alignbit_b32 v30, v31, v27, v29
	v_alignbit_b32 v25, v27, v25, v29
	v_alignbit_b32 v26, v30, v25, 9
	v_ffbh_u32_e32 v27, v26
	v_min_u32_e32 v27, 32, v27
	v_lshrrev_b32_e32 v32, 29, v6
	v_not_b32_e32 v29, v27
	v_alignbit_b32 v25, v26, v25, v29
	v_lshlrev_b32_e32 v26, 31, v32
	v_or_b32_e32 v29, 0x33000000, v26
	v_add_lshl_u32 v27, v27, v28, 23
	v_lshrrev_b32_e32 v25, 9, v25
	v_sub_u32_e32 v27, v29, v27
	v_or_b32_e32 v26, 0.5, v26
	v_lshlrev_b32_e32 v28, 23, v28
	v_or_b32_e32 v25, v27, v25
	v_lshrrev_b32_e32 v27, 9, v30
	v_sub_u32_e32 v26, v26, v28
	v_or_b32_e32 v26, v27, v26
	v_mul_f32_e32 v27, 0x3fc90fda, v26
	v_fma_f32 v28, v26, s34, -v27
	v_fmac_f32_e32 v28, 0x33a22168, v26
	v_fmac_f32_e32 v28, 0x3fc90fda, v25
	v_lshrrev_b32_e32 v6, 30, v6
	v_add_f32_e32 v25, v27, v28
	v_add_u32_e32 v6, v34, v6
